# P6a+P6b epilogues: gate / T rows of later groups touched after the first group's loads (L2 prefetch); on top of v6
# baseline (speedup 1.0000x reference)
.LBB0_1041:
	ds_read_b128 v[0:3], v193
	ds_read_b128 v[4:7], v197
	ds_read_b128 v[8:11], v198
	ds_read_b128 v[12:15], v199
	s_add_u32 s28, s26, 0x80
	s_addc_u32 s29, s27, 0
	s_cmp_eq_u32 s59, 4
	s_cselect_b32 s31, s19, s29
	s_cselect_b32 s30, s55, s28
	s_cselect_b32 s29, s21, s58
	s_cselect_b32 s28, s56, s57
	v_lshl_add_u64 v[160:161], s[26:27], 0, v[158:159]
	s_add_i32 m0, s1, 0xc000
	ds_read_b128 v[164:167], v210
	ds_read_b128 v[168:171], v210 offset:1024
	ds_read_b128 v[172:175], v210 offset:2048
	ds_read_b128 v[176:179], v210 offset:3072
	ds_read_b128 v[180:183], v210 offset:4096
	ds_read_b128 v[184:187], v210 offset:5120
	ds_read_b128 v[214:217], v210 offset:6144
	ds_read_b128 v[218:221], v210 offset:7168
	global_load_lds_dwordx4 v[160:161], off
	v_lshl_add_u64 v[160:161], s[26:27], 0, v[156:157]
	s_add_i32 m0, s1, 0xe000
	s_nop 0
	global_load_lds_dwordx4 v[160:161], off
	s_waitcnt lgkmcnt(8)
	s_barrier
	s_waitcnt lgkmcnt(0)
	s_setprio 1
	s_waitcnt lgkmcnt(0)
	v_mfma_scale_f32_16x16x128_f8f6f4 v[140:143], v[0:7], v[164:171], v[140:143], v211, v212 op_sel_hi:[0,0,0]
	v_mfma_scale_f32_16x16x128_f8f6f4 v[136:139], v[8:15], v[164:171], v[136:139], v211, v212 op_sel_hi:[0,0,0]
	v_mfma_scale_f32_16x16x128_f8f6f4 v[132:135], v[0:7], v[172:179], v[132:135], v211, v212 op_sel_hi:[0,0,0]
	v_mfma_scale_f32_16x16x128_f8f6f4 v[128:131], v[8:15], v[172:179], v[128:131], v211, v212 op_sel_hi:[0,0,0]
	v_mfma_scale_f32_16x16x128_f8f6f4 v[124:127], v[0:7], v[180:187], v[124:127], v211, v212 op_sel_hi:[0,0,0]
	v_mfma_scale_f32_16x16x128_f8f6f4 v[120:123], v[8:15], v[180:187], v[120:123], v211, v212 op_sel_hi:[0,0,0]
	v_mfma_scale_f32_16x16x128_f8f6f4 v[116:119], v[0:7], v[214:221], v[116:119], v211, v212 op_sel_hi:[0,0,0]
	v_mfma_scale_f32_16x16x128_f8f6f4 v[112:115], v[8:15], v[214:221], v[112:115], v211, v212 op_sel_hi:[0,0,0]
	s_setprio 0
	s_barrier
	s_mov_b32 m0, s38
	v_lshl_add_u64 v[160:161], s[28:29], 0, v[144:145]
	ds_read_b128 v[222:225], v194
	ds_read_b128 v[226:229], v200
	ds_read_b128 v[230:233], v201
	ds_read_b128 v[234:237], v202
	global_load_lds_dwordx4 v[160:161], off
	v_lshl_add_u64 v[162:163], s[28:29], 0, v[146:147]
	s_mov_b32 m0, s39
	s_nop 0
	global_load_lds_dwordx4 v[162:163], off
	s_barrier
	s_waitcnt lgkmcnt(0)
	s_setprio 1
	s_waitcnt lgkmcnt(0)
	v_mfma_scale_f32_16x16x128_f8f6f4 v[108:111], v[222:229], v[164:171], v[108:111], v211, v212 op_sel_hi:[0,0,0]
	v_mfma_scale_f32_16x16x128_f8f6f4 v[104:107], v[230:237], v[164:171], v[104:107], v211, v212 op_sel_hi:[0,0,0]
	v_mfma_scale_f32_16x16x128_f8f6f4 v[100:103], v[222:229], v[172:179], v[100:103], v211, v212 op_sel_hi:[0,0,0]
	v_mfma_scale_f32_16x16x128_f8f6f4 v[96:99], v[230:237], v[172:179], v[96:99], v211, v212 op_sel_hi:[0,0,0]
	v_mfma_scale_f32_16x16x128_f8f6f4 v[92:95], v[222:229], v[180:187], v[92:95], v211, v212 op_sel_hi:[0,0,0]
	v_mfma_scale_f32_16x16x128_f8f6f4 v[88:91], v[230:237], v[180:187], v[88:91], v211, v212 op_sel_hi:[0,0,0]
	v_mfma_scale_f32_16x16x128_f8f6f4 v[84:87], v[222:229], v[214:221], v[84:87], v211, v212 op_sel_hi:[0,0,0]
	v_mfma_scale_f32_16x16x128_f8f6f4 v[80:83], v[230:237], v[214:221], v[80:83], v211, v212 op_sel_hi:[0,0,0]
	s_setprio 0
	s_mov_b32 m0, s1
	v_lshl_add_u64 v[164:165], s[30:31], 0, v[148:149]
	s_barrier
	ds_read_b128 v[168:171], v210 offset:16384
	ds_read_b128 v[172:175], v210 offset:17408
	ds_read_b128 v[176:179], v210 offset:18432
	ds_read_b128 v[180:183], v210 offset:19456
	ds_read_b128 v[184:187], v210 offset:20480
	ds_read_b128 v[188:191], v210 offset:21504
	ds_read_b128 v[214:217], v210 offset:22528
	ds_read_b128 v[218:221], v210 offset:23552
	global_load_lds_dwordx4 v[164:165], off
	v_lshl_add_u64 v[166:167], s[30:31], 0, v[150:151]
	s_mov_b32 m0, s40
	s_nop 0
	global_load_lds_dwordx4 v[166:167], off
	s_barrier
	s_waitcnt lgkmcnt(0)
	s_setprio 1
	s_waitcnt lgkmcnt(0)
	v_mfma_scale_f32_16x16x128_f8f6f4 v[76:79], v[0:7], v[168:175], v[76:79], v211, v212 op_sel_hi:[0,0,0]
	v_mfma_scale_f32_16x16x128_f8f6f4 v[72:75], v[8:15], v[168:175], v[72:75], v211, v212 op_sel_hi:[0,0,0]
	v_mfma_scale_f32_16x16x128_f8f6f4 v[68:71], v[0:7], v[176:183], v[68:71], v211, v212 op_sel_hi:[0,0,0]
	v_mfma_scale_f32_16x16x128_f8f6f4 v[64:67], v[8:15], v[176:183], v[64:67], v211, v212 op_sel_hi:[0,0,0]
	v_mfma_scale_f32_16x16x128_f8f6f4 v[60:63], v[0:7], v[184:191], v[60:63], v211, v212 op_sel_hi:[0,0,0]
	v_mfma_scale_f32_16x16x128_f8f6f4 v[56:59], v[8:15], v[184:191], v[56:59], v211, v212 op_sel_hi:[0,0,0]
	v_mfma_scale_f32_16x16x128_f8f6f4 v[52:55], v[0:7], v[214:221], v[52:55], v211, v212 op_sel_hi:[0,0,0]
	v_mfma_scale_f32_16x16x128_f8f6f4 v[48:51], v[8:15], v[214:221], v[48:51], v211, v212 op_sel_hi:[0,0,0]
	s_setprio 0
	s_barrier
	s_add_u32 s60, s28, 0x20000
	s_addc_u32 s61, s29, 0
	s_mov_b32 m0, s41
	v_lshl_add_u64 v[0:1], s[60:61], 0, v[144:145]
	global_load_lds_dwordx4 v[0:1], off
	v_lshl_add_u64 v[0:1], s[60:61], 0, v[146:147]
	s_mov_b32 m0, s42
	s_nop 0
	global_load_lds_dwordx4 v[0:1], off
	s_waitcnt vmcnt(6)
	s_barrier
	s_setprio 1
	v_mfma_scale_f32_16x16x128_f8f6f4 v[44:47], v[222:229], v[168:175], v[44:47], v211, v212 op_sel_hi:[0,0,0]
	v_mfma_scale_f32_16x16x128_f8f6f4 v[40:43], v[230:237], v[168:175], v[40:43], v211, v212 op_sel_hi:[0,0,0]
	v_mfma_scale_f32_16x16x128_f8f6f4 v[36:39], v[222:229], v[176:183], v[36:39], v211, v212 op_sel_hi:[0,0,0]
	v_mfma_scale_f32_16x16x128_f8f6f4 v[32:35], v[230:237], v[176:183], v[32:35], v211, v212 op_sel_hi:[0,0,0]
	v_mfma_scale_f32_16x16x128_f8f6f4 v[28:31], v[222:229], v[184:191], v[28:31], v211, v212 op_sel_hi:[0,0,0]
	v_mfma_scale_f32_16x16x128_f8f6f4 v[24:27], v[230:237], v[184:191], v[24:27], v211, v212 op_sel_hi:[0,0,0]
	v_mfma_scale_f32_16x16x128_f8f6f4 v[20:23], v[222:229], v[214:221], v[20:23], v211, v212 op_sel_hi:[0,0,0]
	v_mfma_scale_f32_16x16x128_f8f6f4 v[16:19], v[230:237], v[214:221], v[16:19], v211, v212 op_sel_hi:[0,0,0]
	s_setprio 0
	s_barrier
	ds_read_b128 v[0:3], v195
	ds_read_b128 v[4:7], v203
	ds_read_b128 v[8:11], v204
	ds_read_b128 v[12:15], v205
	s_mov_b32 m0, s43
	v_lshl_add_u64 v[222:223], s[30:31], 0, v[152:153]
	ds_read_b128 v[168:171], v210 offset:32768
	ds_read_b128 v[172:175], v210 offset:33792
	ds_read_b128 v[176:179], v210 offset:34816
	ds_read_b128 v[180:183], v210 offset:35840
	ds_read_b128 v[184:187], v210 offset:36864
	ds_read_b128 v[188:191], v210 offset:37888
	ds_read_b128 v[214:217], v210 offset:38912
	ds_read_b128 v[218:221], v210 offset:39936
	global_load_lds_dwordx4 v[222:223], off
	v_lshl_add_u64 v[222:223], s[30:31], 0, v[154:155]
	s_mov_b32 m0, s44
	s_nop 0
	global_load_lds_dwordx4 v[222:223], off
	s_waitcnt lgkmcnt(8)
	s_barrier
	s_waitcnt lgkmcnt(0)
	s_setprio 1
	s_waitcnt lgkmcnt(0)
	v_mfma_scale_f32_16x16x128_f8f6f4 v[140:143], v[0:7], v[168:175], v[140:143], v211, v212 op_sel_hi:[0,0,0]
	v_mfma_scale_f32_16x16x128_f8f6f4 v[136:139], v[8:15], v[168:175], v[136:139], v211, v212 op_sel_hi:[0,0,0]
	v_mfma_scale_f32_16x16x128_f8f6f4 v[132:135], v[0:7], v[176:183], v[132:135], v211, v212 op_sel_hi:[0,0,0]
	v_mfma_scale_f32_16x16x128_f8f6f4 v[128:131], v[8:15], v[176:183], v[128:131], v211, v212 op_sel_hi:[0,0,0]
	v_mfma_scale_f32_16x16x128_f8f6f4 v[124:127], v[0:7], v[184:191], v[124:127], v211, v212 op_sel_hi:[0,0,0]
	v_mfma_scale_f32_16x16x128_f8f6f4 v[120:123], v[8:15], v[184:191], v[120:123], v211, v212 op_sel_hi:[0,0,0]
	v_mfma_scale_f32_16x16x128_f8f6f4 v[116:119], v[0:7], v[214:221], v[116:119], v211, v212 op_sel_hi:[0,0,0]
	v_mfma_scale_f32_16x16x128_f8f6f4 v[112:115], v[8:15], v[214:221], v[112:115], v211, v212 op_sel_hi:[0,0,0]
	s_setprio 0
	s_barrier
	s_mov_b32 m0, s46
	v_lshl_add_u64 v[160:161], v[160:161], 0, s[12:13]
	ds_read_b128 v[222:225], v196
	ds_read_b128 v[226:229], v206
	ds_read_b128 v[230:233], v207
	ds_read_b128 v[234:237], v208
	global_load_lds_dwordx4 v[160:161], off
	v_lshl_add_u64 v[160:161], v[162:163], 0, s[12:13]
	s_mov_b32 m0, s47
	s_nop 0
	global_load_lds_dwordx4 v[160:161], off
	s_barrier
	s_waitcnt lgkmcnt(0)
	s_setprio 1
	s_waitcnt lgkmcnt(0)
	v_mfma_scale_f32_16x16x128_f8f6f4 v[108:111], v[222:229], v[168:175], v[108:111], v211, v212 op_sel_hi:[0,0,0]
	v_mfma_scale_f32_16x16x128_f8f6f4 v[104:107], v[230:237], v[168:175], v[104:107], v211, v212 op_sel_hi:[0,0,0]
	v_mfma_scale_f32_16x16x128_f8f6f4 v[100:103], v[222:229], v[176:183], v[100:103], v211, v212 op_sel_hi:[0,0,0]
	v_mfma_scale_f32_16x16x128_f8f6f4 v[96:99], v[230:237], v[176:183], v[96:99], v211, v212 op_sel_hi:[0,0,0]
	v_mfma_scale_f32_16x16x128_f8f6f4 v[92:95], v[222:229], v[184:191], v[92:95], v211, v212 op_sel_hi:[0,0,0]
	v_mfma_scale_f32_16x16x128_f8f6f4 v[88:91], v[230:237], v[184:191], v[88:91], v211, v212 op_sel_hi:[0,0,0]
	v_mfma_scale_f32_16x16x128_f8f6f4 v[84:87], v[222:229], v[214:221], v[84:87], v211, v212 op_sel_hi:[0,0,0]
	v_mfma_scale_f32_16x16x128_f8f6f4 v[80:83], v[230:237], v[214:221], v[80:83], v211, v212 op_sel_hi:[0,0,0]
	s_setprio 0
	s_mov_b32 m0, s48
	v_lshl_add_u64 v[160:161], v[164:165], 0, s[12:13]
	s_barrier
	ds_read_b128 v[168:171], v210 offset:49152
	ds_read_b128 v[172:175], v210 offset:50176
	ds_read_b128 v[176:179], v210 offset:51200
	ds_read_b128 v[180:183], v210 offset:52224
	ds_read_b128 v[184:187], v210 offset:53248
	ds_read_b128 v[188:191], v210 offset:54272
	ds_read_b128 v[214:217], v210 offset:55296
	ds_read_b128 v[218:221], v210 offset:56320
	global_load_lds_dwordx4 v[160:161], off
	v_lshl_add_u64 v[160:161], v[166:167], 0, s[12:13]
	s_mov_b32 m0, s49
	s_nop 0
	global_load_lds_dwordx4 v[160:161], off
	s_barrier
	s_waitcnt lgkmcnt(0)
	s_setprio 1
	s_waitcnt lgkmcnt(0)
	v_mfma_scale_f32_16x16x128_f8f6f4 v[76:79], v[0:7], v[168:175], v[76:79], v211, v212 op_sel_hi:[0,0,0]
	v_mfma_scale_f32_16x16x128_f8f6f4 v[72:75], v[8:15], v[168:175], v[72:75], v211, v212 op_sel_hi:[0,0,0]
	v_mfma_scale_f32_16x16x128_f8f6f4 v[68:71], v[0:7], v[176:183], v[68:71], v211, v212 op_sel_hi:[0,0,0]
	v_mfma_scale_f32_16x16x128_f8f6f4 v[64:67], v[8:15], v[176:183], v[64:67], v211, v212 op_sel_hi:[0,0,0]
	v_mfma_scale_f32_16x16x128_f8f6f4 v[60:63], v[0:7], v[184:191], v[60:63], v211, v212 op_sel_hi:[0,0,0]
	v_mfma_scale_f32_16x16x128_f8f6f4 v[56:59], v[8:15], v[184:191], v[56:59], v211, v212 op_sel_hi:[0,0,0]
	v_mfma_scale_f32_16x16x128_f8f6f4 v[52:55], v[0:7], v[214:221], v[52:55], v211, v212 op_sel_hi:[0,0,0]
	v_mfma_scale_f32_16x16x128_f8f6f4 v[48:51], v[8:15], v[214:221], v[48:51], v211, v212 op_sel_hi:[0,0,0]
	s_setprio 0
	s_barrier
	s_add_u32 s28, s28, 0x20080
	s_addc_u32 s29, s29, 0
	s_mov_b32 m0, s50
	v_lshl_add_u64 v[0:1], s[28:29], 0, v[144:145]
	global_load_lds_dwordx4 v[0:1], off
	v_lshl_add_u64 v[0:1], s[28:29], 0, v[146:147]
	s_mov_b32 m0, s51
	s_nop 0
	global_load_lds_dwordx4 v[0:1], off
	s_waitcnt vmcnt(6)
	s_barrier
	s_setprio 1
	v_mfma_scale_f32_16x16x128_f8f6f4 v[44:47], v[222:229], v[168:175], v[44:47], v211, v212 op_sel_hi:[0,0,0]
	v_mfma_scale_f32_16x16x128_f8f6f4 v[40:43], v[230:237], v[168:175], v[40:43], v211, v212 op_sel_hi:[0,0,0]
	v_mfma_scale_f32_16x16x128_f8f6f4 v[36:39], v[222:229], v[176:183], v[36:39], v211, v212 op_sel_hi:[0,0,0]
	v_mfma_scale_f32_16x16x128_f8f6f4 v[32:35], v[230:237], v[176:183], v[32:35], v211, v212 op_sel_hi:[0,0,0]
	v_mfma_scale_f32_16x16x128_f8f6f4 v[28:31], v[222:229], v[184:191], v[28:31], v211, v212 op_sel_hi:[0,0,0]
	v_mfma_scale_f32_16x16x128_f8f6f4 v[24:27], v[230:237], v[184:191], v[24:27], v211, v212 op_sel_hi:[0,0,0]
	v_mfma_scale_f32_16x16x128_f8f6f4 v[20:23], v[222:229], v[214:221], v[20:23], v211, v212 op_sel_hi:[0,0,0]
	v_mfma_scale_f32_16x16x128_f8f6f4 v[16:19], v[230:237], v[214:221], v[16:19], v211, v212 op_sel_hi:[0,0,0]
	s_setprio 0
	s_add_i32 s59, s59, 2
	s_add_u32 s26, s26, 0x100
	s_addc_u32 s27, s27, 0
	s_add_u32 s57, s57, 0x100
	s_addc_u32 s58, s58, 0
	s_cmp_gt_u32 s59, 5
	s_barrier
	s_cbranch_scc0 .LBB0_1041
	v_lshl_add_u32 v162, s0, 8, v192
	v_lshl_or_b32 v160, s54, 8, v209
	v_mov_b64_e32 v[166:167], s[8:9]
	v_ashrrev_i32_e32 v161, 31, v160
	v_mad_i64_i32 v[0:1], s[26:27], v162, s52, v[166:167]
	v_lshlrev_b64 v[164:165], 1, v[160:161]
	v_lshl_add_u64 v[170:171], v[0:1], 0, s[14:15]
	s_nop 15
	s_nop 15
	v_lshl_add_u64 v[0:1], v[170:171], 0, v[164:165]
	global_load_dwordx4 v[214:217], v[0:1], off
	v_ashrrev_i32_e32 v163, 31, v162
	v_lshl_add_u64 v[168:169], s[6:7], 0, v[164:165]
	v_lshlrev_b64 v[172:173], 12, v[162:163]
	v_lshl_add_u64 v[0:1], v[168:169], 0, v[172:173]
	global_load_dwordx4 v[218:221], v[0:1], off
	v_or_b32_e32 v190, 16, v162
	v_mad_i64_i32 v[0:1], s[26:27], v190, s52, v[166:167]
	v_or_b32_e32 v188, 32, v162
	v_ashrrev_i32_e32 v191, 31, v190
	v_lshl_add_u64 v[178:179], v[0:1], 0, s[14:15]
	v_mad_i64_i32 v[2:3], s[26:27], v188, s52, v[166:167]
	v_lshlrev_b64 v[184:185], 12, v[190:191]
	v_lshl_add_u64 v[0:1], v[178:179], 0, v[164:165]
	v_lshl_add_u64 v[180:181], v[2:3], 0, s[14:15]
	v_lshl_add_u64 v[2:3], v[168:169], 0, v[184:185]
	global_load_dwordx4 v[222:225], v[0:1], off
	global_load_dwordx4 v[226:229], v[2:3], off
	v_or_b32_e32 v186, 48, v162
	v_ashrrev_i32_e32 v189, 31, v188
	v_ashrrev_i32_e32 v187, 31, v186
	v_mad_i64_i32 v[4:5], s[26:27], v186, s52, v[166:167]
	v_lshlrev_b64 v[176:177], 12, v[188:189]
	v_lshl_add_u64 v[174:175], v[4:5], 0, s[14:15]
	v_lshlrev_b64 v[182:183], 12, v[186:187]
	v_lshl_add_u64 v[0:1], v[180:181], 0, v[164:165]
	v_lshl_add_u64 v[2:3], v[168:169], 0, v[176:177]
	v_lshl_add_u64 v[4:5], v[174:175], 0, v[164:165]
	v_lshl_add_u64 v[6:7], v[168:169], 0, v[182:183]
	global_load_dwordx4 v[8:11], v[0:1], off
	global_load_dwordx4 v[12:15], v[2:3], off
	s_nop 0
	global_load_dwordx4 v[0:3], v[4:5], off
	s_nop 0
	global_load_dwordx4 v[4:7], v[6:7], off
	v_mov_b32_e32 v245, 0
	v_add_u32_e32 v244, 0, v162
	v_mad_i64_i32 v[246:247], s[26:27], v244, s52, v[166:167]
	v_lshl_add_u64 v[246:247], v[246:247], 0, s[14:15]
	v_lshl_add_u64 v[246:247], v[246:247], 0, v[164:165]
	v_lshlrev_b64 v[248:249], 12, v[244:245]
	v_lshl_add_u64 v[248:249], v[168:169], 0, v[248:249]
	global_load_dword v250, v[246:247], off offset:256
	global_load_dword v250, v[248:249], off offset:256
	v_add_u32_e32 v244, 16, v162
	v_mad_i64_i32 v[246:247], s[26:27], v244, s52, v[166:167]
	v_lshl_add_u64 v[246:247], v[246:247], 0, s[14:15]
	v_lshl_add_u64 v[246:247], v[246:247], 0, v[164:165]
	v_lshlrev_b64 v[248:249], 12, v[244:245]
	v_lshl_add_u64 v[248:249], v[168:169], 0, v[248:249]
	global_load_dword v250, v[246:247], off offset:256
	global_load_dword v250, v[248:249], off offset:256
	v_add_u32_e32 v244, 32, v162
	v_mad_i64_i32 v[246:247], s[26:27], v244, s52, v[166:167]
	v_lshl_add_u64 v[246:247], v[246:247], 0, s[14:15]
	v_lshl_add_u64 v[246:247], v[246:247], 0, v[164:165]
	v_lshlrev_b64 v[248:249], 12, v[244:245]
	v_lshl_add_u64 v[248:249], v[168:169], 0, v[248:249]
	global_load_dword v250, v[246:247], off offset:256
	global_load_dword v250, v[248:249], off offset:256
	v_add_u32_e32 v244, 48, v162
	v_mad_i64_i32 v[246:247], s[26:27], v244, s52, v[166:167]
	v_lshl_add_u64 v[246:247], v[246:247], 0, s[14:15]
	v_lshl_add_u64 v[246:247], v[246:247], 0, v[164:165]
	v_lshlrev_b64 v[248:249], 12, v[244:245]
	v_lshl_add_u64 v[248:249], v[168:169], 0, v[248:249]
	global_load_dword v250, v[246:247], off offset:256
	global_load_dword v250, v[248:249], off offset:256
	v_add_u32_e32 v244, 128, v162
	v_mad_i64_i32 v[246:247], s[26:27], v244, s52, v[166:167]
	v_lshl_add_u64 v[246:247], v[246:247], 0, s[14:15]
	v_lshl_add_u64 v[246:247], v[246:247], 0, v[164:165]
	v_lshlrev_b64 v[248:249], 12, v[244:245]
	v_lshl_add_u64 v[248:249], v[168:169], 0, v[248:249]
	global_load_dword v250, v[246:247], off
	global_load_dword v250, v[248:249], off
	global_load_dword v250, v[246:247], off offset:256
	global_load_dword v250, v[248:249], off offset:256
	v_add_u32_e32 v244, 144, v162
	v_mad_i64_i32 v[246:247], s[26:27], v244, s52, v[166:167]
	v_lshl_add_u64 v[246:247], v[246:247], 0, s[14:15]
	v_lshl_add_u64 v[246:247], v[246:247], 0, v[164:165]
	v_lshlrev_b64 v[248:249], 12, v[244:245]
	v_lshl_add_u64 v[248:249], v[168:169], 0, v[248:249]
	global_load_dword v250, v[246:247], off
	global_load_dword v250, v[248:249], off
	global_load_dword v250, v[246:247], off offset:256
	global_load_dword v250, v[248:249], off offset:256
	v_add_u32_e32 v244, 160, v162
	v_mad_i64_i32 v[246:247], s[26:27], v244, s52, v[166:167]
	v_lshl_add_u64 v[246:247], v[246:247], 0, s[14:15]
	v_lshl_add_u64 v[246:247], v[246:247], 0, v[164:165]
	v_lshlrev_b64 v[248:249], 12, v[244:245]
	v_lshl_add_u64 v[248:249], v[168:169], 0, v[248:249]
	global_load_dword v250, v[246:247], off
	global_load_dword v250, v[248:249], off
	global_load_dword v250, v[246:247], off offset:256
	global_load_dword v250, v[248:249], off offset:256
	v_add_u32_e32 v244, 176, v162
	v_mad_i64_i32 v[246:247], s[26:27], v244, s52, v[166:167]
	v_lshl_add_u64 v[246:247], v[246:247], 0, s[14:15]
	v_lshl_add_u64 v[246:247], v[246:247], 0, v[164:165]
	v_lshlrev_b64 v[248:249], 12, v[244:245]
	v_lshl_add_u64 v[248:249], v[168:169], 0, v[248:249]
	global_load_dword v250, v[246:247], off
	global_load_dword v250, v[248:249], off
	global_load_dword v250, v[246:247], off offset:256
	global_load_dword v250, v[248:249], off offset:256
	s_and_b64 vcc, exec, s[16:17]
	s_mov_b32 s54, s20
	s_mov_b32 s0, s18
	s_mov_b64 s[28:29], s[24:25]
	s_waitcnt vmcnt(0)
	v_lshlrev_b32_e32 v230, 16, v214
	v_and_b32_e32 v231, 0xffff0000, v214
	v_mul_f32_e32 v230, 0xbfb8aa3b, v230
	v_mul_f32_e32 v231, 0xbfb8aa3b, v231
	v_lshlrev_b32_e32 v234, 16, v216
	v_and_b32_e32 v235, 0xffff0000, v216
	v_exp_f32_e32 v230, v230
	v_exp_f32_e32 v231, v231
	v_mul_f32_e32 v234, 0xbfb8aa3b, v234
	v_mul_f32_e32 v235, 0xbfb8aa3b, v235
	v_lshlrev_b32_e32 v232, 16, v215
	v_and_b32_e32 v233, 0xffff0000, v215
	v_exp_f32_e32 v234, v234
	v_exp_f32_e32 v235, v235
	v_mul_f32_e32 v232, 0xbfb8aa3b, v232
	v_mul_f32_e32 v233, 0xbfb8aa3b, v233
	v_lshlrev_b32_e32 v236, 16, v217
	v_and_b32_e32 v237, 0xffff0000, v217
	v_exp_f32_e32 v232, v232
	v_exp_f32_e32 v233, v233
	v_add_f32_e32 v230, 1.0, v230
	v_add_f32_e32 v231, 1.0, v231
	v_mul_f32_e32 v236, 0xbfb8aa3b, v236
	v_mul_f32_e32 v237, 0xbfb8aa3b, v237
	v_rcp_f32_e32 v230, v230
	v_rcp_f32_e32 v231, v231
	v_exp_f32_e32 v236, v236
	v_exp_f32_e32 v237, v237
	v_add_f32_e32 v234, 1.0, v234
	v_add_f32_e32 v235, 1.0, v235
	v_rcp_f32_e32 v234, v234
	v_rcp_f32_e32 v235, v235
	v_lshlrev_b32_e32 v214, 16, v218
	v_and_b32_e32 v215, 0xffff0000, v218
	v_add_f32_e32 v232, 1.0, v232
	v_add_f32_e32 v233, 1.0, v233
	v_rcp_f32_e32 v232, v232
	v_rcp_f32_e32 v233, v233
	v_pk_fma_f32 v[140:141], v[140:141], v[230:231], v[214:215]
	v_lshlrev_b32_e32 v216, 16, v219
	v_and_b32_e32 v217, 0xffff0000, v219
	v_lshlrev_b32_e32 v218, 16, v220
	v_and_b32_e32 v219, 0xffff0000, v220
	v_add_f32_e32 v236, 1.0, v236
	v_add_f32_e32 v237, 1.0, v237
	v_med3_f32 v141, v141, s53, v213
	v_med3_f32 v214, v140, s53, v213
	v_mov_b32_e32 v140, 0
	v_rcp_f32_e32 v236, v236
	v_rcp_f32_e32 v237, v237
	v_pk_fma_f32 v[136:137], v[136:137], v[234:235], v[218:219]
	v_cvt_pk_fp8_f32 v140, v214, v141
	v_med3_f32 v137, v137, s53, v213
	v_med3_f32 v136, v136, s53, v213
	v_mov_b32_e32 v141, 0
	v_pk_fma_f32 v[142:143], v[142:143], v[232:233], v[216:217]
	v_cvt_pk_fp8_f32 v141, v136, v137
	v_lshlrev_b32_e32 v220, 16, v221
	v_and_b32_e32 v221, 0xffff0000, v221
	v_med3_f32 v143, v143, s53, v213
	v_med3_f32 v142, v142, s53, v213
	v_pk_fma_f32 v[138:139], v[138:139], v[236:237], v[220:221]
	v_cvt_pk_fp8_f32 v140, v142, v143 op_sel:[0,0,1]
	v_lshlrev_b32_e32 v143, 16, v222
	v_and_b32_e32 v216, 0xffff0000, v222
	v_med3_f32 v136, v139, s53, v213
	v_med3_f32 v137, v138, s53, v213
	v_mul_f32_e32 v143, 0xbfb8aa3b, v143
	v_mul_f32_e32 v216, 0xbfb8aa3b, v216
	v_cvt_pk_fp8_f32 v141, v137, v136 op_sel:[0,0,1]
	v_lshlrev_b64 v[136:137], 11, v[162:163]
	v_exp_f32_e32 v163, v143
	v_exp_f32_e32 v217, v216
	v_lshlrev_b32_e32 v216, 16, v223
	v_mul_f32_e32 v216, 0xbfb8aa3b, v216
	v_exp_f32_e32 v218, v216
	v_add_f32_e32 v163, 1.0, v163
	v_rcp_f32_e32 v216, v163
	v_add_f32_e32 v163, 1.0, v217
	v_rcp_f32_e32 v217, v163
	v_add_f32_e32 v163, 1.0, v218
	v_and_b32_e32 v218, 0xffff0000, v223
	v_mul_f32_e32 v218, 0xbfb8aa3b, v218
	v_exp_f32_e32 v219, v218
	v_lshlrev_b32_e32 v218, 16, v224
	v_mul_f32_e32 v218, 0xbfb8aa3b, v218
	v_exp_f32_e32 v220, v218
	v_rcp_f32_e32 v218, v163
	v_add_f32_e32 v163, 1.0, v219
	v_rcp_f32_e32 v219, v163
	v_add_f32_e32 v163, 1.0, v220
	v_lshlrev_b32_e32 v221, 16, v225
	v_rcp_f32_e32 v220, v163
	v_and_b32_e32 v163, 0xffff0000, v224
	v_mul_f32_e32 v221, 0xbfb8aa3b, v221
	v_and_b32_e32 v222, 0xffff0000, v225
	v_mul_f32_e32 v163, 0xbfb8aa3b, v163
	v_exp_f32_e32 v221, v221
	v_mul_f32_e32 v222, 0xbfb8aa3b, v222
	v_exp_f32_e32 v163, v163
	v_exp_f32_e32 v223, v222
	v_add_f32_e32 v221, 1.0, v221
	v_rcp_f32_e32 v222, v221
	v_add_f32_e32 v163, 1.0, v163
	v_add_f32_e32 v221, 1.0, v223
	v_rcp_f32_e32 v223, v221
	v_rcp_f32_e32 v221, v163
	v_lshlrev_b32_e32 v138, 16, v226
	v_and_b32_e32 v139, 0xffff0000, v226
	v_lshlrev_b32_e32 v142, 16, v228
	v_and_b32_e32 v143, 0xffff0000, v228
	v_pk_fma_f32 v[132:133], v[132:133], v[216:217], v[138:139]
	v_pk_fma_f32 v[128:129], v[128:129], v[220:221], v[142:143]
	v_med3_f32 v133, v133, s53, v213
	v_med3_f32 v138, v132, s53, v213
	v_mov_b32_e32 v132, 0
	v_lshl_add_u64 v[136:137], s[10:11], 0, v[136:137]
	v_med3_f32 v129, v129, s53, v213
	v_med3_f32 v128, v128, s53, v213
	v_cvt_pk_fp8_f32 v132, v138, v133
	v_mov_b32_e32 v133, 0
	v_lshl_add_u64 v[136:137], v[136:137], 0, v[160:161]
	v_cvt_pk_fp8_f32 v133, v128, v129
	global_store_dwordx2 v[136:137], v[140:141], off
	v_lshlrev_b32_e32 v140, 16, v227
	v_and_b32_e32 v141, 0xffff0000, v227
	v_lshlrev_b32_e32 v214, 16, v229
	v_and_b32_e32 v215, 0xffff0000, v229
	v_pk_fma_f32 v[134:135], v[134:135], v[218:219], v[140:141]
	v_pk_fma_f32 v[130:131], v[130:131], v[222:223], v[214:215]
	v_med3_f32 v135, v135, s53, v213
	v_med3_f32 v134, v134, s53, v213
	v_med3_f32 v128, v131, s53, v213
	v_med3_f32 v129, v130, s53, v213
	v_cvt_pk_fp8_f32 v132, v134, v135 op_sel:[0,0,1]
	v_cvt_pk_fp8_f32 v133, v129, v128 op_sel:[0,0,1]
	v_lshlrev_b64 v[128:129], 11, v[190:191]
	v_lshl_add_u64 v[128:129], s[10:11], 0, v[128:129]
	v_lshl_add_u64 v[128:129], v[128:129], 0, v[160:161]
	global_store_dwordx2 v[128:129], v[132:133], off
	v_lshlrev_b32_e32 v133, 16, v8
	v_and_b32_e32 v8, 0xffff0000, v8
	v_mul_f32_e32 v8, 0xbfb8aa3b, v8
	v_lshlrev_b32_e32 v135, 16, v9
	v_exp_f32_e32 v8, v8
	v_mul_f32_e32 v135, 0xbfb8aa3b, v135
	v_exp_f32_e32 v138, v135
	v_and_b32_e32 v9, 0xffff0000, v9
	v_add_f32_e32 v8, 1.0, v8
	v_mul_f32_e32 v133, 0xbfb8aa3b, v133
	v_rcp_f32_e32 v135, v8
	v_add_f32_e32 v8, 1.0, v138
	v_mul_f32_e32 v9, 0xbfb8aa3b, v9
	v_lshlrev_b32_e32 v138, 16, v10
	v_and_b32_e32 v10, 0xffff0000, v10
	v_lshlrev_b32_e32 v139, 16, v11
	v_and_b32_e32 v11, 0xffff0000, v11
	v_exp_f32_e32 v134, v133
	v_exp_f32_e32 v9, v9
	v_mul_f32_e32 v138, 0xbfb8aa3b, v138
	v_mul_f32_e32 v10, 0xbfb8aa3b, v10
	v_mul_f32_e32 v139, 0xbfb8aa3b, v139
	v_mul_f32_e32 v11, 0xbfb8aa3b, v11
	v_exp_f32_e32 v138, v138
	v_exp_f32_e32 v10, v10
	v_exp_f32_e32 v139, v139
	v_exp_f32_e32 v11, v11
	v_add_f32_e32 v134, 1.0, v134
	v_add_f32_e32 v9, 1.0, v9
	v_rcp_f32_e32 v134, v134
	v_rcp_f32_e32 v8, v8
	v_rcp_f32_e32 v9, v9
	v_add_f32_e32 v138, 1.0, v138
	v_add_f32_e32 v140, 1.0, v10
	v_add_f32_e32 v10, 1.0, v139
	v_add_f32_e32 v11, 1.0, v11
	v_rcp_f32_e32 v138, v138
	v_rcp_f32_e32 v10, v10
	v_rcp_f32_e32 v11, v11
	v_rcp_f32_e32 v139, v140
	v_lshlrev_b32_e32 v130, 16, v12
	v_and_b32_e32 v131, 0xffff0000, v12
	v_lshlrev_b32_e32 v12, 16, v13
	v_and_b32_e32 v13, 0xffff0000, v13
	v_lshlrev_b32_e32 v132, 16, v14
	v_and_b32_e32 v133, 0xffff0000, v14
	v_lshlrev_b32_e32 v14, 16, v15
	v_and_b32_e32 v15, 0xffff0000, v15
	v_pk_fma_f32 v[8:9], v[126:127], v[8:9], v[12:13]
	v_pk_fma_f32 v[12:13], v[124:125], v[134:135], v[130:131]
	v_pk_fma_f32 v[10:11], v[122:123], v[10:11], v[14:15]
	v_pk_fma_f32 v[14:15], v[120:121], v[138:139], v[132:133]
	v_med3_f32 v120, v9, s53, v213
	v_med3_f32 v121, v8, s53, v213
	v_med3_f32 v9, v13, s53, v213
	v_med3_f32 v12, v12, s53, v213
	v_mov_b32_e32 v8, 0
	v_med3_f32 v13, v15, s53, v213
	v_med3_f32 v14, v14, s53, v213
	v_cvt_pk_fp8_f32 v8, v12, v9
	v_mov_b32_e32 v9, 0
	v_cvt_pk_fp8_f32 v9, v14, v13
	v_med3_f32 v11, v11, s53, v213
	v_med3_f32 v10, v10, s53, v213
	v_lshlrev_b32_e32 v13, 16, v1
	v_cvt_pk_fp8_f32 v9, v10, v11 op_sel:[0,0,1]
	v_lshlrev_b64 v[10:11], 11, v[188:189]
	v_lshl_add_u64 v[10:11], s[10:11], 0, v[10:11]
	v_lshl_add_u64 v[14:15], v[10:11], 0, v[160:161]
	v_lshlrev_b32_e32 v11, 16, v0
	v_and_b32_e32 v0, 0xffff0000, v0
	v_mul_f32_e32 v0, 0xbfb8aa3b, v0
	v_exp_f32_e32 v0, v0
	v_mul_f32_e32 v13, 0xbfb8aa3b, v13
	v_cvt_pk_fp8_f32 v8, v121, v120 op_sel:[0,0,1]
	v_exp_f32_e32 v120, v13
	v_add_f32_e32 v0, 1.0, v0
	v_and_b32_e32 v1, 0xffff0000, v1
	v_mul_f32_e32 v11, 0xbfb8aa3b, v11
	v_rcp_f32_e32 v13, v0
	v_add_f32_e32 v0, 1.0, v120
	v_mul_f32_e32 v1, 0xbfb8aa3b, v1
	v_lshlrev_b32_e32 v120, 16, v2
	v_and_b32_e32 v2, 0xffff0000, v2
	v_lshlrev_b32_e32 v121, 16, v3
	v_and_b32_e32 v3, 0xffff0000, v3
	v_exp_f32_e32 v12, v11
	v_exp_f32_e32 v1, v1
	v_mul_f32_e32 v120, 0xbfb8aa3b, v120
	v_mul_f32_e32 v2, 0xbfb8aa3b, v2
	v_mul_f32_e32 v121, 0xbfb8aa3b, v121
	v_mul_f32_e32 v3, 0xbfb8aa3b, v3
	v_exp_f32_e32 v120, v120
	v_exp_f32_e32 v2, v2
	v_exp_f32_e32 v121, v121
	v_exp_f32_e32 v3, v3
	v_add_f32_e32 v12, 1.0, v12
	v_add_f32_e32 v1, 1.0, v1
	v_rcp_f32_e32 v12, v12
	v_rcp_f32_e32 v0, v0
	v_rcp_f32_e32 v1, v1
	v_add_f32_e32 v120, 1.0, v120
	v_add_f32_e32 v122, 1.0, v2
	v_add_f32_e32 v2, 1.0, v121
	v_add_f32_e32 v3, 1.0, v3
	v_rcp_f32_e32 v120, v120
	v_rcp_f32_e32 v2, v2
	v_rcp_f32_e32 v3, v3
	v_rcp_f32_e32 v121, v122
	global_store_dwordx2 v[14:15], v[8:9], off
	v_lshlrev_b32_e32 v8, 16, v4
	v_and_b32_e32 v9, 0xffff0000, v4
	v_lshlrev_b32_e32 v4, 16, v5
	v_and_b32_e32 v5, 0xffff0000, v5
	v_lshlrev_b32_e32 v10, 16, v6
	v_and_b32_e32 v11, 0xffff0000, v6
	v_lshlrev_b32_e32 v6, 16, v7
	v_and_b32_e32 v7, 0xffff0000, v7
	v_pk_fma_f32 v[0:1], v[118:119], v[0:1], v[4:5]
	v_pk_fma_f32 v[4:5], v[116:117], v[12:13], v[8:9]
	v_pk_fma_f32 v[2:3], v[114:115], v[2:3], v[6:7]
	v_pk_fma_f32 v[6:7], v[112:113], v[120:121], v[10:11]
	v_med3_f32 v8, v1, s53, v213
	v_med3_f32 v9, v0, s53, v213
	v_med3_f32 v1, v5, s53, v213
	v_med3_f32 v4, v4, s53, v213
	v_mov_b32_e32 v0, 0
	v_med3_f32 v5, v7, s53, v213
	v_med3_f32 v6, v6, s53, v213
	v_cvt_pk_fp8_f32 v0, v4, v1
	v_mov_b32_e32 v1, 0
	v_cvt_pk_fp8_f32 v1, v6, v5
	v_med3_f32 v3, v3, s53, v213
	v_med3_f32 v2, v2, s53, v213
	v_cvt_pk_fp8_f32 v0, v9, v8 op_sel:[0,0,1]
	v_cvt_pk_fp8_f32 v1, v2, v3 op_sel:[0,0,1]
	v_lshlrev_b64 v[2:3], 11, v[186:187]
	v_lshl_add_u64 v[2:3], s[10:11], 0, v[2:3]
	v_lshl_add_u64 v[112:113], v[2:3], 0, v[160:161]
	global_store_dwordx2 v[112:113], v[0:1], off
	v_or_b32_e32 v0, 0x80, v160
	v_ashrrev_i32_e32 v1, 31, v0
	v_lshlrev_b64 v[12:13], 1, v[0:1]
	v_lshl_add_u64 v[0:1], s[6:7], 0, v[172:173]
	v_lshl_add_u64 v[0:1], v[0:1], 0, v[12:13]
	global_load_dwordx4 v[114:117], v[0:1], off
	v_lshl_add_u64 v[0:1], v[170:171], 0, v[12:13]
	global_load_dwordx4 v[118:121], v[0:1], off
	v_lshl_add_u64 v[0:1], s[6:7], 0, v[184:185]
	v_lshl_add_u64 v[0:1], v[0:1], 0, v[12:13]
	global_load_dwordx4 v[122:125], v[0:1], off
	v_lshl_add_u64 v[0:1], v[178:179], 0, v[12:13]
	global_load_dwordx4 v[130:133], v[0:1], off
	v_lshl_add_u64 v[0:1], v[180:181], 0, v[12:13]
	v_lshl_add_u64 v[2:3], s[6:7], 0, v[176:177]
	v_lshl_add_u64 v[2:3], v[2:3], 0, v[12:13]
	global_load_dwordx4 v[8:11], v[0:1], off
	global_load_dwordx4 v[138:141], v[2:3], off
	v_lshl_add_u64 v[2:3], s[6:7], 0, v[182:183]
	v_lshl_add_u64 v[0:1], v[174:175], 0, v[12:13]
	v_lshl_add_u64 v[4:5], v[2:3], 0, v[12:13]
	global_load_dwordx4 v[0:3], v[0:1], off
	s_nop 0
	global_load_dwordx4 v[4:7], v[4:5], off
	s_waitcnt vmcnt(0)
	v_lshlrev_b32_e32 v126, 16, v114
	v_and_b32_e32 v127, 0xffff0000, v114
	v_lshlrev_b32_e32 v135, 16, v118
	v_and_b32_e32 v118, 0xffff0000, v118
	v_mul_f32_e32 v118, 0xbfb8aa3b, v118
	v_lshlrev_b32_e32 v143, 16, v119
	v_exp_f32_e32 v118, v118
	v_mul_f32_e32 v143, 0xbfb8aa3b, v143
	v_exp_f32_e32 v163, v143
	v_mul_f32_e32 v135, 0xbfb8aa3b, v135
	v_add_f32_e32 v118, 1.0, v118
	v_rcp_f32_e32 v143, v118
	v_add_f32_e32 v118, 1.0, v163
	v_lshlrev_b32_e32 v163, 16, v120
	v_mul_f32_e32 v163, 0xbfb8aa3b, v163
	v_and_b32_e32 v120, 0xffff0000, v120
	v_and_b32_e32 v119, 0xffff0000, v119
	v_exp_f32_e32 v163, v163
	v_mul_f32_e32 v120, 0xbfb8aa3b, v120
	v_exp_f32_e32 v142, v135
	v_mul_f32_e32 v119, 0xbfb8aa3b, v119
	v_exp_f32_e32 v120, v120
	v_exp_f32_e32 v119, v119
	v_add_f32_e32 v163, 1.0, v163
	v_add_f32_e32 v142, 1.0, v142
	v_rcp_f32_e32 v170, v163
	v_lshlrev_b32_e32 v163, 16, v121
	v_and_b32_e32 v121, 0xffff0000, v121
	v_add_f32_e32 v171, 1.0, v120
	v_rcp_f32_e32 v142, v142
	v_add_f32_e32 v119, 1.0, v119
	v_mul_f32_e32 v163, 0xbfb8aa3b, v163
	v_mul_f32_e32 v121, 0xbfb8aa3b, v121
	v_rcp_f32_e32 v171, v171
	v_rcp_f32_e32 v118, v118
	v_rcp_f32_e32 v119, v119
	v_exp_f32_e32 v163, v163
	v_exp_f32_e32 v121, v121
	v_lshlrev_b32_e32 v134, 16, v116
	v_and_b32_e32 v135, 0xffff0000, v116
	v_lshlrev_b32_e32 v114, 16, v115
	v_and_b32_e32 v115, 0xffff0000, v115
	v_pk_fma_f32 v[108:109], v[108:109], v[142:143], v[126:127]
	v_pk_fma_f32 v[104:105], v[104:105], v[170:171], v[134:135]
	v_add_f32_e32 v120, 1.0, v163
	v_add_f32_e32 v121, 1.0, v121
	v_pk_fma_f32 v[110:111], v[110:111], v[118:119], v[114:115]
	v_med3_f32 v109, v109, s53, v213
	v_med3_f32 v108, v108, s53, v213
	v_med3_f32 v115, v104, s53, v213
	v_mov_b32_e32 v104, 0
	v_rcp_f32_e32 v120, v120
	v_rcp_f32_e32 v121, v121
	v_cvt_pk_fp8_f32 v104, v108, v109
	v_lshlrev_b32_e32 v116, 16, v117
	v_and_b32_e32 v117, 0xffff0000, v117
	v_med3_f32 v111, v111, s53, v213
	v_med3_f32 v110, v110, s53, v213
	v_pk_fma_f32 v[106:107], v[106:107], v[120:121], v[116:117]
	v_cvt_pk_fp8_f32 v104, v110, v111 op_sel:[0,0,1]
	v_lshlrev_b32_e32 v111, 16, v130
	v_and_b32_e32 v117, 0xffff0000, v130
	v_lshlrev_b32_e32 v120, 16, v132
	v_and_b32_e32 v121, 0xffff0000, v132
	v_mul_f32_e32 v111, 0xbfb8aa3b, v111
	v_mul_f32_e32 v117, 0xbfb8aa3b, v117
	v_mul_f32_e32 v120, 0xbfb8aa3b, v120
	v_mul_f32_e32 v121, 0xbfb8aa3b, v121
	v_exp_f32_e32 v116, v111
	v_exp_f32_e32 v117, v117
	v_exp_f32_e32 v120, v120
	v_exp_f32_e32 v121, v121
	v_lshlrev_b32_e32 v118, 16, v131
	v_and_b32_e32 v119, 0xffff0000, v131
	v_med3_f32 v114, v105, s53, v213
	v_mov_b32_e32 v105, 0
	v_mul_f32_e32 v118, 0xbfb8aa3b, v118
	v_mul_f32_e32 v119, 0xbfb8aa3b, v119
	v_cvt_pk_fp8_f32 v105, v115, v114
	v_add_f32_e32 v116, 1.0, v116
	v_exp_f32_e32 v118, v118
	v_add_f32_e32 v117, 1.0, v117
	v_exp_f32_e32 v119, v119
	v_add_f32_e32 v120, 1.0, v120
	v_add_f32_e32 v121, 1.0, v121
	v_rcp_f32_e32 v116, v116
	v_rcp_f32_e32 v117, v117
	v_rcp_f32_e32 v120, v120
	v_rcp_f32_e32 v121, v121
	v_med3_f32 v107, v107, s53, v213
	v_med3_f32 v106, v106, s53, v213
	v_cvt_pk_fp8_f32 v105, v106, v107 op_sel:[0,0,1]
	v_lshlrev_b32_e32 v106, 16, v122
	v_and_b32_e32 v107, 0xffff0000, v122
	v_lshlrev_b32_e32 v110, 16, v124
	v_and_b32_e32 v111, 0xffff0000, v124
	v_add_f32_e32 v118, 1.0, v118
	v_add_f32_e32 v119, 1.0, v119
	v_rcp_f32_e32 v118, v118
	v_rcp_f32_e32 v119, v119
	v_pk_fma_f32 v[100:101], v[100:101], v[116:117], v[106:107]
	v_pk_fma_f32 v[96:97], v[96:97], v[120:121], v[110:111]
	v_med3_f32 v101, v101, s53, v213
	v_med3_f32 v100, v100, s53, v213
	v_med3_f32 v107, v96, s53, v213
	v_mov_b32_e32 v96, 0
	v_cvt_pk_fp8_f32 v96, v100, v101
	v_lshlrev_b32_e32 v108, 16, v123
	v_and_b32_e32 v109, 0xffff0000, v123
	v_pk_fma_f32 v[102:103], v[102:103], v[118:119], v[108:109]
	v_lshlrev_b32_e32 v109, 16, v9
	v_med3_f32 v103, v103, s53, v213
	v_med3_f32 v102, v102, s53, v213
	v_cvt_pk_fp8_f32 v96, v102, v103 op_sel:[0,0,1]
	v_lshlrev_b32_e32 v103, 16, v8
	v_and_b32_e32 v8, 0xffff0000, v8
	v_mul_f32_e32 v8, 0xbfb8aa3b, v8
	v_lshlrev_b32_e32 v122, 16, v133
	v_and_b32_e32 v123, 0xffff0000, v133
	v_exp_f32_e32 v8, v8
	v_mul_f32_e32 v109, 0xbfb8aa3b, v109
	v_mul_f32_e32 v122, 0xbfb8aa3b, v122
	v_mul_f32_e32 v123, 0xbfb8aa3b, v123
	v_exp_f32_e32 v110, v109
	v_exp_f32_e32 v122, v122
	v_exp_f32_e32 v123, v123
	v_add_f32_e32 v8, 1.0, v8
	v_and_b32_e32 v9, 0xffff0000, v9
	v_mul_f32_e32 v103, 0xbfb8aa3b, v103
	v_rcp_f32_e32 v109, v8
	v_add_f32_e32 v8, 1.0, v110
	v_mul_f32_e32 v9, 0xbfb8aa3b, v9
	v_lshlrev_b32_e32 v110, 16, v10
	v_and_b32_e32 v10, 0xffff0000, v10
	v_lshlrev_b32_e32 v111, 16, v11
	v_and_b32_e32 v11, 0xffff0000, v11
	v_add_f32_e32 v122, 1.0, v122
	v_add_f32_e32 v123, 1.0, v123
	v_exp_f32_e32 v108, v103
	v_exp_f32_e32 v9, v9
	v_mul_f32_e32 v10, 0xbfb8aa3b, v10
	v_mul_f32_e32 v111, 0xbfb8aa3b, v111
	v_mul_f32_e32 v11, 0xbfb8aa3b, v11
	v_rcp_f32_e32 v122, v122
	v_rcp_f32_e32 v123, v123
	v_exp_f32_e32 v10, v10
	v_exp_f32_e32 v111, v111
	v_exp_f32_e32 v11, v11
	v_mul_f32_e32 v110, 0xbfb8aa3b, v110
	v_med3_f32 v106, v97, s53, v213
	v_mov_b32_e32 v97, 0
	v_exp_f32_e32 v110, v110
	v_lshlrev_b32_e32 v114, 16, v125
	v_and_b32_e32 v115, 0xffff0000, v125
	v_cvt_pk_fp8_f32 v97, v107, v106
	v_add_f32_e32 v108, 1.0, v108
	v_add_f32_e32 v9, 1.0, v9
	v_pk_fma_f32 v[98:99], v[98:99], v[122:123], v[114:115]
	v_rcp_f32_e32 v108, v108
	v_rcp_f32_e32 v8, v8
	v_rcp_f32_e32 v9, v9
	v_add_f32_e32 v114, 1.0, v10
	v_add_f32_e32 v10, 1.0, v111
	v_add_f32_e32 v11, 1.0, v11
	v_rcp_f32_e32 v10, v10
	v_rcp_f32_e32 v11, v11
	v_med3_f32 v99, v99, s53, v213
	v_med3_f32 v98, v98, s53, v213
	v_add_f32_e32 v110, 1.0, v110
	v_cvt_pk_fp8_f32 v97, v98, v99 op_sel:[0,0,1]
	v_lshlrev_b32_e32 v98, 16, v138
	v_and_b32_e32 v99, 0xffff0000, v138
	v_lshlrev_b32_e32 v100, 16, v139
	v_and_b32_e32 v101, 0xffff0000, v139
	v_rcp_f32_e32 v110, v110
	v_rcp_f32_e32 v111, v114
	v_lshlrev_b32_e32 v106, 16, v141
	v_and_b32_e32 v107, 0xffff0000, v141
	v_pk_fma_f32 v[8:9], v[94:95], v[8:9], v[100:101]
	v_pk_fma_f32 v[92:93], v[92:93], v[108:109], v[98:99]
	v_pk_fma_f32 v[10:11], v[90:91], v[10:11], v[106:107]
	v_med3_f32 v90, v9, s53, v213
	v_med3_f32 v91, v8, s53, v213
	v_med3_f32 v9, v93, s53, v213
	v_med3_f32 v92, v92, s53, v213
	v_mov_b32_e32 v8, 0
	v_lshlrev_b32_e32 v102, 16, v140
	v_and_b32_e32 v103, 0xffff0000, v140
	v_cvt_pk_fp8_f32 v8, v92, v9
	v_pk_fma_f32 v[88:89], v[88:89], v[110:111], v[102:103]
	v_mov_b32_e32 v9, 0
	v_med3_f32 v89, v89, s53, v213
	v_med3_f32 v88, v88, s53, v213
	v_cvt_pk_fp8_f32 v9, v88, v89
	v_lshlrev_b32_e32 v89, 16, v0
	v_and_b32_e32 v0, 0xffff0000, v0
	v_cvt_pk_fp8_f32 v8, v91, v90 op_sel:[0,0,1]
	v_mul_f32_e32 v0, 0xbfb8aa3b, v0
	v_lshlrev_b32_e32 v91, 16, v1
	v_exp_f32_e32 v0, v0
	v_mul_f32_e32 v91, 0xbfb8aa3b, v91
	v_exp_f32_e32 v92, v91
	v_and_b32_e32 v1, 0xffff0000, v1
	v_add_f32_e32 v0, 1.0, v0
	v_mul_f32_e32 v89, 0xbfb8aa3b, v89
	v_rcp_f32_e32 v91, v0
	v_add_f32_e32 v0, 1.0, v92
	v_mul_f32_e32 v1, 0xbfb8aa3b, v1
	v_lshlrev_b32_e32 v92, 16, v2
	v_and_b32_e32 v2, 0xffff0000, v2
	v_lshlrev_b32_e32 v93, 16, v3
	v_and_b32_e32 v3, 0xffff0000, v3
	v_exp_f32_e32 v90, v89
	v_exp_f32_e32 v1, v1
	v_mul_f32_e32 v92, 0xbfb8aa3b, v92
	v_mul_f32_e32 v2, 0xbfb8aa3b, v2
	v_mul_f32_e32 v93, 0xbfb8aa3b, v93
	v_mul_f32_e32 v3, 0xbfb8aa3b, v3
	v_exp_f32_e32 v92, v92
	v_exp_f32_e32 v2, v2
	v_exp_f32_e32 v93, v93
	v_exp_f32_e32 v3, v3
	v_add_f32_e32 v90, 1.0, v90
	v_add_f32_e32 v1, 1.0, v1
	v_rcp_f32_e32 v90, v90
	v_rcp_f32_e32 v0, v0
	v_rcp_f32_e32 v1, v1
	v_add_f32_e32 v92, 1.0, v92
	v_add_f32_e32 v94, 1.0, v2
	v_add_f32_e32 v2, 1.0, v93
	v_add_f32_e32 v3, 1.0, v3
	v_rcp_f32_e32 v92, v92
	v_rcp_f32_e32 v2, v2
	v_rcp_f32_e32 v3, v3
	v_rcp_f32_e32 v93, v94
	v_med3_f32 v11, v11, s53, v213
	v_med3_f32 v10, v10, s53, v213
	v_cvt_pk_fp8_f32 v9, v10, v11 op_sel:[0,0,1]
	v_lshlrev_b32_e32 v10, 16, v4
	v_and_b32_e32 v11, 0xffff0000, v4
	v_lshlrev_b32_e32 v4, 16, v5
	v_and_b32_e32 v5, 0xffff0000, v5
	v_lshlrev_b32_e32 v88, 16, v6
	v_and_b32_e32 v89, 0xffff0000, v6
	v_lshlrev_b32_e32 v6, 16, v7
	v_and_b32_e32 v7, 0xffff0000, v7
	v_pk_fma_f32 v[0:1], v[86:87], v[0:1], v[4:5]
	v_pk_fma_f32 v[4:5], v[84:85], v[90:91], v[10:11]
	v_pk_fma_f32 v[2:3], v[82:83], v[2:3], v[6:7]
	v_pk_fma_f32 v[6:7], v[80:81], v[92:93], v[88:89]
	v_med3_f32 v10, v1, s53, v213
	v_med3_f32 v11, v0, s53, v213
	v_med3_f32 v1, v5, s53, v213
	v_med3_f32 v4, v4, s53, v213
	v_mov_b32_e32 v0, 0
	v_med3_f32 v5, v7, s53, v213
	v_med3_f32 v6, v6, s53, v213
	v_cvt_pk_fp8_f32 v0, v4, v1
	v_mov_b32_e32 v1, 0
	v_cvt_pk_fp8_f32 v1, v6, v5
	v_med3_f32 v3, v3, s53, v213
	v_med3_f32 v2, v2, s53, v213
	v_cvt_pk_fp8_f32 v0, v11, v10 op_sel:[0,0,1]
	v_cvt_pk_fp8_f32 v1, v2, v3 op_sel:[0,0,1]
	global_store_dwordx2 v[136:137], v[104:105], off offset:128
	global_store_dwordx2 v[128:129], v[96:97], off offset:128
	global_store_dwordx2 v[14:15], v[8:9], off offset:128
	global_store_dwordx2 v[112:113], v[0:1], off offset:128
	v_add_u32_e32 v14, 0x80, v162
	v_ashrrev_i32_e32 v15, 31, v14
	v_lshlrev_b64 v[80:81], 12, v[14:15]
	v_lshl_add_u64 v[0:1], v[168:169], 0, v[80:81]
	global_load_dwordx4 v[100:103], v[0:1], off
	v_mad_i64_i32 v[0:1], s[26:27], v14, s52, v[166:167]
	v_lshl_add_u64 v[82:83], v[0:1], 0, s[14:15]
	v_lshl_add_u64 v[0:1], v[82:83], 0, v[164:165]
	global_load_dwordx4 v[104:107], v[0:1], off
	v_add_u32_e32 v120, 0x90, v162
	v_mad_i64_i32 v[0:1], s[26:27], v120, s52, v[166:167]
	v_ashrrev_i32_e32 v121, 31, v120
	v_lshl_add_u64 v[84:85], v[0:1], 0, s[14:15]
	v_lshl_add_u64 v[0:1], v[84:85], 0, v[164:165]
	v_lshlrev_b64 v[86:87], 12, v[120:121]
	v_lshl_add_u64 v[2:3], v[168:169], 0, v[86:87]
	global_load_dwordx4 v[108:111], v[0:1], off
	global_load_dwordx4 v[112:115], v[2:3], off
	v_add_u32_e32 v98, 0xa0, v162
	v_mad_i64_i32 v[0:1], s[26:27], v98, s52, v[166:167]
	v_ashrrev_i32_e32 v99, 31, v98
	v_lshl_add_u64 v[88:89], v[0:1], 0, s[14:15]
	v_lshl_add_u64 v[0:1], v[88:89], 0, v[164:165]
	v_lshlrev_b64 v[90:91], 12, v[98:99]
	v_lshl_add_u64 v[2:3], v[168:169], 0, v[90:91]
	global_load_dwordx4 v[8:11], v[0:1], off
	global_load_dwordx4 v[116:119], v[2:3], off
	v_add_u32_e32 v96, 0xb0, v162
	v_ashrrev_i32_e32 v97, 31, v96
	v_mad_i64_i32 v[0:1], s[26:27], v96, s52, v[166:167]
	v_lshl_add_u64 v[92:93], v[0:1], 0, s[14:15]
	v_lshlrev_b64 v[94:95], 12, v[96:97]
	v_lshl_add_u64 v[0:1], v[92:93], 0, v[164:165]
	v_lshl_add_u64 v[4:5], v[168:169], 0, v[94:95]
	global_load_dwordx4 v[0:3], v[0:1], off
	s_nop 0
	global_load_dwordx4 v[4:7], v[4:5], off
	v_lshlrev_b64 v[14:15], 11, v[14:15]
	v_lshl_add_u64 v[14:15], s[10:11], 0, v[14:15]
	v_lshl_add_u64 v[14:15], v[14:15], 0, v[160:161]
	s_mov_b64 s[26:27], s[22:23]
	s_waitcnt vmcnt(0)
	v_lshlrev_b32_e32 v122, 16, v100
	v_and_b32_e32 v123, 0xffff0000, v100
	v_lshlrev_b32_e32 v124, 16, v102
	v_lshlrev_b32_e32 v100, 16, v101
	v_and_b32_e32 v101, 0xffff0000, v101
	v_lshlrev_b32_e32 v125, 16, v104
	v_and_b32_e32 v104, 0xffff0000, v104
	v_mul_f32_e32 v104, 0xbfb8aa3b, v104
	v_lshlrev_b32_e32 v127, 16, v105
	v_exp_f32_e32 v104, v104
	v_mul_f32_e32 v127, 0xbfb8aa3b, v127
	v_exp_f32_e32 v128, v127
	v_mul_f32_e32 v125, 0xbfb8aa3b, v125
	v_add_f32_e32 v104, 1.0, v104
	v_rcp_f32_e32 v127, v104
	v_add_f32_e32 v104, 1.0, v128
	v_lshlrev_b32_e32 v128, 16, v106
	v_and_b32_e32 v106, 0xffff0000, v106
	v_and_b32_e32 v105, 0xffff0000, v105
	v_mul_f32_e32 v128, 0xbfb8aa3b, v128
	v_mul_f32_e32 v106, 0xbfb8aa3b, v106
	v_lshlrev_b32_e32 v129, 16, v107
	v_exp_f32_e32 v126, v125
	v_mul_f32_e32 v105, 0xbfb8aa3b, v105
	v_exp_f32_e32 v128, v128
	v_exp_f32_e32 v106, v106
	v_mul_f32_e32 v129, 0xbfb8aa3b, v129
	v_exp_f32_e32 v105, v105
	v_exp_f32_e32 v129, v129
	v_add_f32_e32 v126, 1.0, v126
	v_add_f32_e32 v128, 1.0, v128
	v_and_b32_e32 v107, 0xffff0000, v107
	v_add_f32_e32 v130, 1.0, v106
	v_rcp_f32_e32 v126, v126
	v_add_f32_e32 v105, 1.0, v105
	v_rcp_f32_e32 v128, v128
	v_mul_f32_e32 v107, 0xbfb8aa3b, v107
	v_add_f32_e32 v106, 1.0, v129
	v_rcp_f32_e32 v129, v130
	v_rcp_f32_e32 v104, v104
	v_rcp_f32_e32 v105, v105
	v_exp_f32_e32 v107, v107
	v_and_b32_e32 v125, 0xffff0000, v102
	v_pk_fma_f32 v[76:77], v[76:77], v[126:127], v[122:123]
	v_pk_fma_f32 v[72:73], v[72:73], v[128:129], v[124:125]
	v_add_f32_e32 v107, 1.0, v107
	v_pk_fma_f32 v[78:79], v[78:79], v[104:105], v[100:101]
	v_med3_f32 v77, v77, s53, v213
	v_med3_f32 v76, v76, s53, v213
	v_med3_f32 v100, v73, s53, v213
	v_med3_f32 v101, v72, s53, v213
	v_mov_b32_e32 v72, 0
	v_mov_b32_e32 v73, 0
	v_rcp_f32_e32 v106, v106
	v_rcp_f32_e32 v107, v107
	v_cvt_pk_fp8_f32 v72, v76, v77
	v_cvt_pk_fp8_f32 v73, v101, v100
	v_lshlrev_b32_e32 v77, 16, v108
	v_and_b32_e32 v101, 0xffff0000, v108
	v_mul_f32_e32 v77, 0xbfb8aa3b, v77
	v_mul_f32_e32 v101, 0xbfb8aa3b, v101
	v_exp_f32_e32 v100, v77
	v_exp_f32_e32 v101, v101
	v_lshlrev_b32_e32 v102, 16, v103
	v_and_b32_e32 v103, 0xffff0000, v103
	v_pk_fma_f32 v[74:75], v[74:75], v[106:107], v[102:103]
	v_lshlrev_b32_e32 v102, 16, v109
	v_and_b32_e32 v103, 0xffff0000, v109
	v_med3_f32 v79, v79, s53, v213
	v_med3_f32 v78, v78, s53, v213
	v_med3_f32 v75, v75, s53, v213
	v_med3_f32 v74, v74, s53, v213
	v_mul_f32_e32 v102, 0xbfb8aa3b, v102
	v_mul_f32_e32 v103, 0xbfb8aa3b, v103
	v_cvt_pk_fp8_f32 v72, v78, v79 op_sel:[0,0,1]
	v_cvt_pk_fp8_f32 v73, v74, v75 op_sel:[0,0,1]
	v_add_f32_e32 v100, 1.0, v100
	v_exp_f32_e32 v102, v102
	v_add_f32_e32 v101, 1.0, v101
	v_exp_f32_e32 v103, v103
	v_rcp_f32_e32 v100, v100
	v_rcp_f32_e32 v101, v101
	v_lshlrev_b32_e32 v104, 16, v110
	v_and_b32_e32 v105, 0xffff0000, v110
	global_store_dwordx2 v[14:15], v[72:73], off
	v_lshlrev_b32_e32 v72, 16, v112
	v_and_b32_e32 v73, 0xffff0000, v112
	v_add_f32_e32 v102, 1.0, v102
	v_mul_f32_e32 v104, 0xbfb8aa3b, v104
	v_add_f32_e32 v103, 1.0, v103
	v_mul_f32_e32 v105, 0xbfb8aa3b, v105
	v_exp_f32_e32 v104, v104
	v_rcp_f32_e32 v102, v102
	v_rcp_f32_e32 v103, v103
	v_exp_f32_e32 v105, v105
	v_pk_fma_f32 v[68:69], v[68:69], v[100:101], v[72:73]
	v_lshlrev_b32_e32 v74, 16, v113
	v_med3_f32 v69, v69, s53, v213
	v_med3_f32 v72, v68, s53, v213
	v_mov_b32_e32 v68, 0
	v_cvt_pk_fp8_f32 v68, v72, v69
	v_and_b32_e32 v75, 0xffff0000, v113
	v_add_f32_e32 v104, 1.0, v104
	v_add_f32_e32 v105, 1.0, v105
	v_pk_fma_f32 v[70:71], v[70:71], v[102:103], v[74:75]
	v_rcp_f32_e32 v104, v104
	v_lshlrev_b32_e32 v106, 16, v111
	v_and_b32_e32 v107, 0xffff0000, v111
	v_rcp_f32_e32 v105, v105
	v_med3_f32 v71, v71, s53, v213
	v_med3_f32 v70, v70, s53, v213
	v_mul_f32_e32 v106, 0xbfb8aa3b, v106
	v_mul_f32_e32 v107, 0xbfb8aa3b, v107
	v_cvt_pk_fp8_f32 v68, v70, v71 op_sel:[0,0,1]
	v_lshlrev_b32_e32 v71, 16, v8
	v_and_b32_e32 v8, 0xffff0000, v8
	v_exp_f32_e32 v106, v106
	v_exp_f32_e32 v107, v107
	v_mul_f32_e32 v8, 0xbfb8aa3b, v8
	v_lshlrev_b32_e32 v75, 16, v9
	v_lshlrev_b32_e32 v76, 16, v114
	v_and_b32_e32 v77, 0xffff0000, v114
	v_exp_f32_e32 v8, v8
	v_mul_f32_e32 v75, 0xbfb8aa3b, v75
	v_pk_fma_f32 v[64:65], v[64:65], v[104:105], v[76:77]
	v_exp_f32_e32 v76, v75
	v_add_f32_e32 v106, 1.0, v106
	v_add_f32_e32 v107, 1.0, v107
	v_rcp_f32_e32 v106, v106
	v_rcp_f32_e32 v107, v107
	v_add_f32_e32 v8, 1.0, v8
	v_and_b32_e32 v9, 0xffff0000, v9
	v_med3_f32 v65, v65, s53, v213
	v_med3_f32 v64, v64, s53, v213
	v_mov_b32_e32 v69, 0
	v_mul_f32_e32 v71, 0xbfb8aa3b, v71
	v_rcp_f32_e32 v75, v8
	v_add_f32_e32 v8, 1.0, v76
	v_mul_f32_e32 v9, 0xbfb8aa3b, v9
	v_lshlrev_b32_e32 v76, 16, v10
	v_and_b32_e32 v10, 0xffff0000, v10
	v_lshlrev_b32_e32 v77, 16, v11
	v_and_b32_e32 v11, 0xffff0000, v11
	v_cvt_pk_fp8_f32 v69, v64, v65
	v_exp_f32_e32 v74, v71
	v_exp_f32_e32 v9, v9
	v_mul_f32_e32 v76, 0xbfb8aa3b, v76
	v_mul_f32_e32 v10, 0xbfb8aa3b, v10
	v_mul_f32_e32 v77, 0xbfb8aa3b, v77
	v_mul_f32_e32 v11, 0xbfb8aa3b, v11
	v_lshlrev_b32_e32 v78, 16, v115
	v_and_b32_e32 v79, 0xffff0000, v115
	v_exp_f32_e32 v76, v76
	v_exp_f32_e32 v10, v10
	v_exp_f32_e32 v77, v77
	v_exp_f32_e32 v11, v11
	v_pk_fma_f32 v[66:67], v[66:67], v[106:107], v[78:79]
	v_add_f32_e32 v74, 1.0, v74
	v_med3_f32 v64, v67, s53, v213
	v_med3_f32 v65, v66, s53, v213
	v_cvt_pk_fp8_f32 v69, v65, v64 op_sel:[0,0,1]
	v_add_f32_e32 v9, 1.0, v9
	v_lshlrev_b64 v[64:65], 11, v[120:121]
	v_rcp_f32_e32 v74, v74
	v_rcp_f32_e32 v8, v8
	v_rcp_f32_e32 v9, v9
	v_add_f32_e32 v76, 1.0, v76
	v_add_f32_e32 v78, 1.0, v10
	v_add_f32_e32 v10, 1.0, v77
	v_add_f32_e32 v11, 1.0, v11
	v_lshl_add_u64 v[64:65], s[10:11], 0, v[64:65]
	v_rcp_f32_e32 v76, v76
	v_rcp_f32_e32 v10, v10
	v_rcp_f32_e32 v11, v11
	v_rcp_f32_e32 v77, v78
	v_lshl_add_u64 v[64:65], v[64:65], 0, v[160:161]
	global_store_dwordx2 v[64:65], v[68:69], off
	v_lshlrev_b32_e32 v66, 16, v116
	v_and_b32_e32 v67, 0xffff0000, v116
	v_lshlrev_b32_e32 v68, 16, v117
	v_and_b32_e32 v69, 0xffff0000, v117
	v_lshlrev_b32_e32 v70, 16, v118
	v_and_b32_e32 v71, 0xffff0000, v118
	v_lshlrev_b32_e32 v72, 16, v119
	v_and_b32_e32 v73, 0xffff0000, v119
	v_pk_fma_f32 v[8:9], v[62:63], v[8:9], v[68:69]
	v_pk_fma_f32 v[60:61], v[60:61], v[74:75], v[66:67]
	v_pk_fma_f32 v[10:11], v[58:59], v[10:11], v[72:73]
	v_pk_fma_f32 v[56:57], v[56:57], v[76:77], v[70:71]
	v_med3_f32 v58, v9, s53, v213
	v_med3_f32 v59, v8, s53, v213
	v_med3_f32 v9, v61, s53, v213
	v_med3_f32 v60, v60, s53, v213
	v_mov_b32_e32 v8, 0
	v_med3_f32 v57, v57, s53, v213
	v_med3_f32 v56, v56, s53, v213
	v_cvt_pk_fp8_f32 v8, v60, v9
	v_mov_b32_e32 v9, 0
	v_cvt_pk_fp8_f32 v9, v56, v57
	v_med3_f32 v11, v11, s53, v213
	v_med3_f32 v10, v10, s53, v213
	v_cvt_pk_fp8_f32 v8, v59, v58 op_sel:[0,0,1]
	v_cvt_pk_fp8_f32 v9, v10, v11 op_sel:[0,0,1]
	v_lshlrev_b64 v[10:11], 11, v[98:99]
	v_lshl_add_u64 v[10:11], s[10:11], 0, v[10:11]
	v_lshl_add_u64 v[56:57], v[10:11], 0, v[160:161]
	v_lshlrev_b32_e32 v11, 16, v0
	v_and_b32_e32 v0, 0xffff0000, v0
	v_mul_f32_e32 v0, 0xbfb8aa3b, v0
	v_lshlrev_b32_e32 v59, 16, v1
	v_exp_f32_e32 v0, v0
	v_mul_f32_e32 v59, 0xbfb8aa3b, v59
	v_exp_f32_e32 v60, v59
	v_and_b32_e32 v1, 0xffff0000, v1
	v_add_f32_e32 v0, 1.0, v0
	v_mul_f32_e32 v11, 0xbfb8aa3b, v11
	v_rcp_f32_e32 v59, v0
	v_add_f32_e32 v0, 1.0, v60
	v_mul_f32_e32 v1, 0xbfb8aa3b, v1
	v_lshlrev_b32_e32 v60, 16, v2
	v_and_b32_e32 v2, 0xffff0000, v2
	v_lshlrev_b32_e32 v61, 16, v3
	v_and_b32_e32 v3, 0xffff0000, v3
	v_exp_f32_e32 v58, v11
	v_exp_f32_e32 v1, v1
	v_mul_f32_e32 v60, 0xbfb8aa3b, v60
	v_mul_f32_e32 v2, 0xbfb8aa3b, v2
	v_mul_f32_e32 v61, 0xbfb8aa3b, v61
	v_mul_f32_e32 v3, 0xbfb8aa3b, v3
	v_exp_f32_e32 v60, v60
	v_exp_f32_e32 v2, v2
	v_exp_f32_e32 v61, v61
	v_exp_f32_e32 v3, v3
	v_add_f32_e32 v58, 1.0, v58
	v_add_f32_e32 v1, 1.0, v1
	v_rcp_f32_e32 v58, v58
	v_rcp_f32_e32 v0, v0
	v_rcp_f32_e32 v1, v1
	v_add_f32_e32 v60, 1.0, v60
	v_add_f32_e32 v62, 1.0, v2
	v_add_f32_e32 v2, 1.0, v61
	v_add_f32_e32 v3, 1.0, v3
	v_rcp_f32_e32 v60, v60
	v_rcp_f32_e32 v2, v2
	v_rcp_f32_e32 v3, v3
	v_rcp_f32_e32 v61, v62
	global_store_dwordx2 v[56:57], v[8:9], off
	v_lshlrev_b32_e32 v8, 16, v4
	v_and_b32_e32 v9, 0xffff0000, v4
	v_lshlrev_b32_e32 v4, 16, v5
	v_and_b32_e32 v5, 0xffff0000, v5
	v_lshlrev_b32_e32 v10, 16, v6
	v_and_b32_e32 v11, 0xffff0000, v6
	v_lshlrev_b32_e32 v6, 16, v7
	v_and_b32_e32 v7, 0xffff0000, v7
	v_pk_fma_f32 v[0:1], v[54:55], v[0:1], v[4:5]
	v_pk_fma_f32 v[4:5], v[52:53], v[58:59], v[8:9]
	v_pk_fma_f32 v[2:3], v[50:51], v[2:3], v[6:7]
	v_pk_fma_f32 v[6:7], v[48:49], v[60:61], v[10:11]
	v_med3_f32 v8, v1, s53, v213
	v_med3_f32 v9, v0, s53, v213
	v_med3_f32 v1, v5, s53, v213
	v_med3_f32 v4, v4, s53, v213
	v_mov_b32_e32 v0, 0
	v_med3_f32 v5, v7, s53, v213
	v_med3_f32 v6, v6, s53, v213
	v_cvt_pk_fp8_f32 v0, v4, v1
	v_mov_b32_e32 v1, 0
	v_cvt_pk_fp8_f32 v1, v6, v5
	v_med3_f32 v3, v3, s53, v213
	v_med3_f32 v2, v2, s53, v213
	v_cvt_pk_fp8_f32 v0, v9, v8 op_sel:[0,0,1]
	v_cvt_pk_fp8_f32 v1, v2, v3 op_sel:[0,0,1]
	v_lshlrev_b64 v[2:3], 11, v[96:97]
	v_lshl_add_u64 v[2:3], s[10:11], 0, v[2:3]
	v_lshl_add_u64 v[48:49], v[2:3], 0, v[160:161]
	global_store_dwordx2 v[48:49], v[0:1], off
	v_lshl_add_u64 v[0:1], s[6:7], 0, v[80:81]
	v_lshl_add_u64 v[0:1], v[0:1], 0, v[12:13]
	global_load_dwordx4 v[50:53], v[0:1], off
	v_lshl_add_u64 v[0:1], v[82:83], 0, v[12:13]
	global_load_dwordx4 v[58:61], v[0:1], off
	v_lshl_add_u64 v[0:1], s[6:7], 0, v[86:87]
	v_lshl_add_u64 v[0:1], v[0:1], 0, v[12:13]
	global_load_dwordx4 v[66:69], v[0:1], off
	v_lshl_add_u64 v[0:1], v[84:85], 0, v[12:13]
	global_load_dwordx4 v[70:73], v[0:1], off
	v_lshl_add_u64 v[0:1], v[88:89], 0, v[12:13]
	v_lshl_add_u64 v[2:3], s[6:7], 0, v[90:91]
	v_lshl_add_u64 v[2:3], v[2:3], 0, v[12:13]
	global_load_dwordx4 v[8:11], v[0:1], off
	global_load_dwordx4 v[74:77], v[2:3], off
	v_lshl_add_u64 v[2:3], s[6:7], 0, v[94:95]
	v_lshl_add_u64 v[0:1], v[92:93], 0, v[12:13]
	v_lshl_add_u64 v[4:5], v[2:3], 0, v[12:13]
	global_load_dwordx4 v[0:3], v[0:1], off
	s_nop 0
	global_load_dwordx4 v[4:7], v[4:5], off
	s_waitcnt vmcnt(0)
	v_lshlrev_b32_e32 v12, 16, v50
	v_and_b32_e32 v13, 0xffff0000, v50
	v_lshlrev_b32_e32 v55, 16, v58
	v_and_b32_e32 v58, 0xffff0000, v58
	v_mul_f32_e32 v58, 0xbfb8aa3b, v58
	v_lshlrev_b32_e32 v63, 16, v59
	v_and_b32_e32 v59, 0xffff0000, v59
	v_mul_f32_e32 v55, 0xbfb8aa3b, v55
	v_exp_f32_e32 v58, v58
	v_mul_f32_e32 v63, 0xbfb8aa3b, v63
	v_mul_f32_e32 v59, 0xbfb8aa3b, v59
	v_exp_f32_e32 v62, v55
	v_exp_f32_e32 v78, v63
	v_exp_f32_e32 v59, v59
	v_add_f32_e32 v58, 1.0, v58
	v_add_f32_e32 v62, 1.0, v62
	v_rcp_f32_e32 v63, v58
	v_add_f32_e32 v58, 1.0, v78
	v_lshlrev_b32_e32 v78, 16, v60
	v_add_f32_e32 v59, 1.0, v59
	v_and_b32_e32 v60, 0xffff0000, v60
	v_rcp_f32_e32 v62, v62
	v_mul_f32_e32 v78, 0xbfb8aa3b, v78
	v_rcp_f32_e32 v58, v58
	v_rcp_f32_e32 v59, v59
	v_mul_f32_e32 v60, 0xbfb8aa3b, v60
	v_lshlrev_b32_e32 v79, 16, v61
	v_exp_f32_e32 v78, v78
	v_exp_f32_e32 v60, v60
	v_mul_f32_e32 v79, 0xbfb8aa3b, v79
	v_exp_f32_e32 v79, v79
	v_lshlrev_b32_e32 v50, 16, v51
	v_and_b32_e32 v51, 0xffff0000, v51
	v_and_b32_e32 v61, 0xffff0000, v61
	v_mul_f32_e32 v61, 0xbfb8aa3b, v61
	v_pk_fma_f32 v[46:47], v[46:47], v[58:59], v[50:51]
	v_pk_fma_f32 v[12:13], v[44:45], v[62:63], v[12:13]
	v_add_f32_e32 v78, 1.0, v78
	v_exp_f32_e32 v61, v61
	v_add_f32_e32 v80, 1.0, v60
	v_med3_f32 v45, v46, s53, v213
	v_med3_f32 v13, v13, s53, v213
	v_med3_f32 v46, v12, s53, v213
	v_mov_b32_e32 v12, 0
	v_rcp_f32_e32 v78, v78
	v_add_f32_e32 v60, 1.0, v79
	v_rcp_f32_e32 v79, v80
	v_cvt_pk_fp8_f32 v12, v46, v13
	v_lshlrev_b32_e32 v54, 16, v52
	v_and_b32_e32 v55, 0xffff0000, v52
	v_add_f32_e32 v61, 1.0, v61
	v_med3_f32 v44, v47, s53, v213
	v_rcp_f32_e32 v60, v60
	v_rcp_f32_e32 v61, v61
	v_pk_fma_f32 v[40:41], v[40:41], v[78:79], v[54:55]
	v_cvt_pk_fp8_f32 v12, v45, v44 op_sel:[0,0,1]
	v_lshlrev_b32_e32 v45, 16, v70
	v_and_b32_e32 v51, 0xffff0000, v70
	v_lshlrev_b32_e32 v54, 16, v72
	v_and_b32_e32 v55, 0xffff0000, v72
	v_mul_f32_e32 v45, 0xbfb8aa3b, v45
	v_mul_f32_e32 v51, 0xbfb8aa3b, v51
	v_mul_f32_e32 v54, 0xbfb8aa3b, v54
	v_mul_f32_e32 v55, 0xbfb8aa3b, v55
	v_exp_f32_e32 v50, v45
	v_exp_f32_e32 v51, v51
	v_exp_f32_e32 v54, v54
	v_exp_f32_e32 v55, v55
	v_lshlrev_b32_e32 v52, 16, v53
	v_and_b32_e32 v53, 0xffff0000, v53
	v_pk_fma_f32 v[42:43], v[42:43], v[60:61], v[52:53]
	v_lshlrev_b32_e32 v52, 16, v71
	v_and_b32_e32 v53, 0xffff0000, v71
	v_med3_f32 v41, v41, s53, v213
	v_med3_f32 v40, v40, s53, v213
	v_mov_b32_e32 v13, 0
	v_mul_f32_e32 v52, 0xbfb8aa3b, v52
	v_mul_f32_e32 v53, 0xbfb8aa3b, v53
	v_cvt_pk_fp8_f32 v13, v40, v41
	v_add_f32_e32 v50, 1.0, v50
	v_exp_f32_e32 v52, v52
	v_add_f32_e32 v51, 1.0, v51
	v_exp_f32_e32 v53, v53
	v_add_f32_e32 v54, 1.0, v54
	v_add_f32_e32 v55, 1.0, v55
	v_rcp_f32_e32 v50, v50
	v_rcp_f32_e32 v51, v51
	v_rcp_f32_e32 v54, v54
	v_rcp_f32_e32 v55, v55
	v_med3_f32 v40, v43, s53, v213
	v_med3_f32 v41, v42, s53, v213
	v_cvt_pk_fp8_f32 v13, v41, v40 op_sel:[0,0,1]
	v_lshlrev_b32_e32 v40, 16, v66
	v_and_b32_e32 v41, 0xffff0000, v66
	v_lshlrev_b32_e32 v44, 16, v68
	v_and_b32_e32 v45, 0xffff0000, v68
	v_add_f32_e32 v52, 1.0, v52
	v_add_f32_e32 v53, 1.0, v53
	v_rcp_f32_e32 v52, v52
	v_rcp_f32_e32 v53, v53
	v_pk_fma_f32 v[36:37], v[36:37], v[50:51], v[40:41]
	v_pk_fma_f32 v[32:33], v[32:33], v[54:55], v[44:45]
	v_med3_f32 v37, v37, s53, v213
	v_med3_f32 v36, v36, s53, v213
	v_med3_f32 v41, v32, s53, v213
	v_mov_b32_e32 v32, 0
	v_cvt_pk_fp8_f32 v32, v36, v37
	v_lshlrev_b32_e32 v42, 16, v67
	v_and_b32_e32 v43, 0xffff0000, v67
	v_pk_fma_f32 v[38:39], v[38:39], v[52:53], v[42:43]
	v_lshlrev_b32_e32 v43, 16, v9
	v_med3_f32 v39, v39, s53, v213
	v_med3_f32 v38, v38, s53, v213
	v_cvt_pk_fp8_f32 v32, v38, v39 op_sel:[0,0,1]
	v_lshlrev_b32_e32 v39, 16, v8
	v_and_b32_e32 v8, 0xffff0000, v8
	v_mul_f32_e32 v8, 0xbfb8aa3b, v8
	v_lshlrev_b32_e32 v58, 16, v73
	v_and_b32_e32 v59, 0xffff0000, v73
	v_exp_f32_e32 v8, v8
	v_mul_f32_e32 v43, 0xbfb8aa3b, v43
	v_mul_f32_e32 v58, 0xbfb8aa3b, v58
	v_mul_f32_e32 v59, 0xbfb8aa3b, v59
	v_exp_f32_e32 v44, v43
	v_exp_f32_e32 v58, v58
	v_exp_f32_e32 v59, v59
	v_add_f32_e32 v8, 1.0, v8
	v_and_b32_e32 v9, 0xffff0000, v9
	v_mul_f32_e32 v39, 0xbfb8aa3b, v39
	v_rcp_f32_e32 v43, v8
	v_add_f32_e32 v8, 1.0, v44
	v_mul_f32_e32 v9, 0xbfb8aa3b, v9
	v_lshlrev_b32_e32 v44, 16, v10
	v_and_b32_e32 v10, 0xffff0000, v10
	v_lshlrev_b32_e32 v45, 16, v11
	v_and_b32_e32 v11, 0xffff0000, v11
	v_add_f32_e32 v58, 1.0, v58
	v_add_f32_e32 v59, 1.0, v59
	v_exp_f32_e32 v42, v39
	v_exp_f32_e32 v9, v9
	v_mul_f32_e32 v10, 0xbfb8aa3b, v10
	v_mul_f32_e32 v45, 0xbfb8aa3b, v45
	v_mul_f32_e32 v11, 0xbfb8aa3b, v11
	v_rcp_f32_e32 v58, v58
	v_rcp_f32_e32 v59, v59
	v_exp_f32_e32 v10, v10
	v_exp_f32_e32 v45, v45
	v_exp_f32_e32 v11, v11
	v_mul_f32_e32 v44, 0xbfb8aa3b, v44
	v_med3_f32 v40, v33, s53, v213
	v_mov_b32_e32 v33, 0
	v_exp_f32_e32 v44, v44
	v_lshlrev_b32_e32 v46, 16, v69
	v_and_b32_e32 v47, 0xffff0000, v69
	v_cvt_pk_fp8_f32 v33, v41, v40
	v_add_f32_e32 v42, 1.0, v42
	v_add_f32_e32 v9, 1.0, v9
	v_pk_fma_f32 v[34:35], v[34:35], v[58:59], v[46:47]
	v_rcp_f32_e32 v42, v42
	v_rcp_f32_e32 v8, v8
	v_rcp_f32_e32 v9, v9
	v_add_f32_e32 v46, 1.0, v10
	v_add_f32_e32 v10, 1.0, v45
	v_add_f32_e32 v11, 1.0, v11
	v_rcp_f32_e32 v10, v10
	v_rcp_f32_e32 v11, v11
	v_med3_f32 v35, v35, s53, v213
	v_med3_f32 v34, v34, s53, v213
	v_add_f32_e32 v44, 1.0, v44
	v_cvt_pk_fp8_f32 v33, v34, v35 op_sel:[0,0,1]
	v_lshlrev_b32_e32 v34, 16, v74
	v_and_b32_e32 v35, 0xffff0000, v74
	v_lshlrev_b32_e32 v36, 16, v75
	v_and_b32_e32 v37, 0xffff0000, v75
	v_rcp_f32_e32 v44, v44
	v_rcp_f32_e32 v45, v46
	v_lshlrev_b32_e32 v40, 16, v77
	v_and_b32_e32 v41, 0xffff0000, v77
	v_pk_fma_f32 v[8:9], v[30:31], v[8:9], v[36:37]
	v_pk_fma_f32 v[28:29], v[28:29], v[42:43], v[34:35]
	v_pk_fma_f32 v[10:11], v[26:27], v[10:11], v[40:41]
	v_med3_f32 v26, v9, s53, v213
	v_med3_f32 v27, v8, s53, v213
	v_med3_f32 v9, v29, s53, v213
	v_med3_f32 v28, v28, s53, v213
	v_mov_b32_e32 v8, 0
	v_lshlrev_b32_e32 v38, 16, v76
	v_and_b32_e32 v39, 0xffff0000, v76
	v_cvt_pk_fp8_f32 v8, v28, v9
	v_pk_fma_f32 v[24:25], v[24:25], v[44:45], v[38:39]
	v_mov_b32_e32 v9, 0
	v_med3_f32 v25, v25, s53, v213
	v_med3_f32 v24, v24, s53, v213
	v_cvt_pk_fp8_f32 v9, v24, v25
	v_lshlrev_b32_e32 v25, 16, v0
	v_and_b32_e32 v0, 0xffff0000, v0
	v_cvt_pk_fp8_f32 v8, v27, v26 op_sel:[0,0,1]
	v_mul_f32_e32 v0, 0xbfb8aa3b, v0
	v_lshlrev_b32_e32 v27, 16, v1
	v_exp_f32_e32 v0, v0
	v_mul_f32_e32 v27, 0xbfb8aa3b, v27
	v_exp_f32_e32 v28, v27
	v_and_b32_e32 v1, 0xffff0000, v1
	v_add_f32_e32 v0, 1.0, v0
	v_mul_f32_e32 v25, 0xbfb8aa3b, v25
	v_rcp_f32_e32 v27, v0
	v_add_f32_e32 v0, 1.0, v28
	v_mul_f32_e32 v1, 0xbfb8aa3b, v1
	v_lshlrev_b32_e32 v28, 16, v2
	v_and_b32_e32 v2, 0xffff0000, v2
	v_lshlrev_b32_e32 v29, 16, v3
	v_and_b32_e32 v3, 0xffff0000, v3
	v_exp_f32_e32 v26, v25
	v_exp_f32_e32 v1, v1
	v_mul_f32_e32 v28, 0xbfb8aa3b, v28
	v_mul_f32_e32 v2, 0xbfb8aa3b, v2
	v_mul_f32_e32 v29, 0xbfb8aa3b, v29
	v_mul_f32_e32 v3, 0xbfb8aa3b, v3
	v_exp_f32_e32 v28, v28
	v_exp_f32_e32 v2, v2
	v_exp_f32_e32 v29, v29
	v_exp_f32_e32 v3, v3
	v_add_f32_e32 v26, 1.0, v26
	v_add_f32_e32 v1, 1.0, v1
	v_rcp_f32_e32 v26, v26
	v_rcp_f32_e32 v0, v0
	v_rcp_f32_e32 v1, v1
	v_add_f32_e32 v28, 1.0, v28
	v_add_f32_e32 v30, 1.0, v2
	v_add_f32_e32 v2, 1.0, v29
	v_add_f32_e32 v3, 1.0, v3
	v_rcp_f32_e32 v28, v28
	v_rcp_f32_e32 v2, v2
	v_rcp_f32_e32 v3, v3
	v_rcp_f32_e32 v29, v30
	v_med3_f32 v11, v11, s53, v213
	v_med3_f32 v10, v10, s53, v213
	v_cvt_pk_fp8_f32 v9, v10, v11 op_sel:[0,0,1]
	v_lshlrev_b32_e32 v10, 16, v4
	v_and_b32_e32 v11, 0xffff0000, v4
	v_lshlrev_b32_e32 v4, 16, v5
	v_and_b32_e32 v5, 0xffff0000, v5
	v_lshlrev_b32_e32 v24, 16, v6
	v_and_b32_e32 v25, 0xffff0000, v6
	v_lshlrev_b32_e32 v6, 16, v7
	v_and_b32_e32 v7, 0xffff0000, v7
	v_pk_fma_f32 v[0:1], v[22:23], v[0:1], v[4:5]
	v_pk_fma_f32 v[4:5], v[20:21], v[26:27], v[10:11]
	v_pk_fma_f32 v[2:3], v[18:19], v[2:3], v[6:7]
	v_pk_fma_f32 v[6:7], v[16:17], v[28:29], v[24:25]
	v_med3_f32 v10, v1, s53, v213
	v_med3_f32 v11, v0, s53, v213
	v_med3_f32 v1, v5, s53, v213
	v_med3_f32 v4, v4, s53, v213
	v_mov_b32_e32 v0, 0
	v_med3_f32 v5, v7, s53, v213
	v_med3_f32 v6, v6, s53, v213
	v_cvt_pk_fp8_f32 v0, v4, v1
	v_mov_b32_e32 v1, 0
	v_cvt_pk_fp8_f32 v1, v6, v5
	v_med3_f32 v3, v3, s53, v213
	v_med3_f32 v2, v2, s53, v213
	v_cvt_pk_fp8_f32 v0, v11, v10 op_sel:[0,0,1]
	v_cvt_pk_fp8_f32 v1, v2, v3 op_sel:[0,0,1]
	global_store_dwordx2 v[14:15], v[12:13], off offset:128
	global_store_dwordx2 v[64:65], v[32:33], off offset:128
	global_store_dwordx2 v[56:57], v[8:9], off offset:128
	global_store_dwordx2 v[48:49], v[0:1], off offset:128
	s_cbranch_vccz .LBB0_1034
	s_waitcnt vmcnt(0)
	s_cmpk_gt_u32 s33, 0xff
	s_cbranch_scc1 .LBB0_1045
	s_barrier
